# GEMM K-loop headers aligned to 64 bytes
# baseline (speedup 1.0000x reference)
.LBB0_212:
	s_add_u32 s12, s12, 0x40080
	s_addc_u32 s13, s13, 0
	s_add_u32 s7, s14, 0x100
	v_mov_b64_e32 v[8:9], v[4:5]
	v_mov_b64_e32 v[20:21], v[4:5]
	v_mov_b64_e32 v[24:25], v[4:5]
	v_mov_b64_e32 v[36:37], v[4:5]
	v_mov_b64_e32 v[40:41], v[4:5]
	v_mov_b64_e32 v[52:53], v[4:5]
	v_mov_b64_e32 v[56:57], v[4:5]
	v_mov_b64_e32 v[12:13], v[4:5]
	v_mov_b64_e32 v[16:17], v[4:5]
	v_mov_b64_e32 v[28:29], v[4:5]
	v_mov_b64_e32 v[32:33], v[4:5]
	v_mov_b64_e32 v[44:45], v[4:5]
	v_mov_b64_e32 v[48:49], v[4:5]
	v_mov_b64_e32 v[60:61], v[4:5]
	v_mov_b64_e32 v[64:65], v[4:5]
	v_mov_b64_e32 v[68:69], v[4:5]
	v_mov_b64_e32 v[72:73], v[4:5]
	v_mov_b64_e32 v[84:85], v[4:5]
	v_mov_b64_e32 v[88:89], v[4:5]
	v_mov_b64_e32 v[100:101], v[4:5]
	v_mov_b64_e32 v[104:105], v[4:5]
	v_mov_b64_e32 v[116:117], v[4:5]
	v_mov_b64_e32 v[120:121], v[4:5]
	v_mov_b64_e32 v[76:77], v[4:5]
	v_mov_b64_e32 v[80:81], v[4:5]
	v_mov_b64_e32 v[92:93], v[4:5]
	v_mov_b64_e32 v[96:97], v[4:5]
	v_mov_b64_e32 v[108:109], v[4:5]
	v_mov_b64_e32 v[112:113], v[4:5]
	v_mov_b64_e32 v[124:125], v[4:5]
	v_mov_b64_e32 v[128:129], v[4:5]
	s_addc_u32 s28, s15, 0
	s_mov_b32 s29, -2
	v_mov_b64_e32 v[6:7], v[2:3]
	v_mov_b64_e32 v[18:19], v[2:3]
	v_mov_b64_e32 v[22:23], v[2:3]
	v_mov_b64_e32 v[34:35], v[2:3]
	v_mov_b64_e32 v[38:39], v[2:3]
	v_mov_b64_e32 v[50:51], v[2:3]
	v_mov_b64_e32 v[54:55], v[2:3]
	v_mov_b64_e32 v[10:11], v[2:3]
	v_mov_b64_e32 v[14:15], v[2:3]
	v_mov_b64_e32 v[26:27], v[2:3]
	v_mov_b64_e32 v[30:31], v[2:3]
	v_mov_b64_e32 v[42:43], v[2:3]
	v_mov_b64_e32 v[46:47], v[2:3]
	v_mov_b64_e32 v[58:59], v[2:3]
	v_mov_b64_e32 v[62:63], v[2:3]
	v_mov_b64_e32 v[66:67], v[2:3]
	v_mov_b64_e32 v[70:71], v[2:3]
	v_mov_b64_e32 v[82:83], v[2:3]
	v_mov_b64_e32 v[86:87], v[2:3]
	v_mov_b64_e32 v[98:99], v[2:3]
	v_mov_b64_e32 v[102:103], v[2:3]
	v_mov_b64_e32 v[114:115], v[2:3]
	v_mov_b64_e32 v[118:119], v[2:3]
	v_mov_b64_e32 v[74:75], v[2:3]
	v_mov_b64_e32 v[78:79], v[2:3]
	v_mov_b64_e32 v[90:91], v[2:3]
	v_mov_b64_e32 v[94:95], v[2:3]
	v_mov_b64_e32 v[106:107], v[2:3]
	v_mov_b64_e32 v[110:111], v[2:3]
	v_mov_b64_e32 v[122:123], v[2:3]
	v_mov_b64_e32 v[126:127], v[2:3]
	.p2align 6

.LBB0_885:
	s_add_u32 s42, s6, 0x100
	s_addc_u32 s43, s7, 0
	s_mov_b32 s46, -2
	.p2align 6

.LBB0_935:
	v_lshrrev_b32_e32 v13, 1, v3
	v_and_b32_e32 v139, 24, v13
	s_lshl_b32 s8, s8, 5
	v_and_b32_e32 v12, 15, v3
	v_lshlrev_b32_e32 v13, 1, v139
	v_lshlrev_b32_e32 v3, 2, v3
	s_and_b32 s28, s8, 0x60
	v_lshl_or_b32 v138, s9, 6, v12
	v_lshl_or_b32 v12, v12, 6, v13
	s_lshl_b32 s9, s9, 13
	v_and_b32_e32 v3, 32, v3
	s_lshl_b32 s8, s28, 7
	v_lshl_add_u64 v[4:5], s[0:1], 0, v[130:131]
	v_mov_b32_e32 v133, v131
	v_bitop3_b32 v140, v12, s8, v3 bitop3:0xde
	s_add_u32 s8, s0, 0x20080
	v_lshl_add_u64 v[6:7], s[0:1], 0, v[132:133]
	v_mov_b32_e32 v137, v131
	v_bitop3_b32 v13, v12, s9, v3 bitop3:0xde
	s_addc_u32 s9, s1, 0
	s_add_i32 m0, s24, 0x18000
	v_lshl_add_u64 v[4:5], v[4:5], 0, s[84:85]
	v_lshl_add_u64 v[8:9], s[40:41], 0, v[136:137]
	v_mov_b32_e32 v135, v131
	s_waitcnt vmcnt(2)
	s_barrier
	global_load_lds_dwordx4 v[4:5], off
	v_lshl_add_u64 v[4:5], v[6:7], 0, s[84:85]
	s_add_i32 m0, s24, 0x1a000
	s_add_i32 s29, s24, 0x8000
	v_lshl_add_u64 v[10:11], s[40:41], 0, v[134:135]
	global_load_lds_dwordx4 v[4:5], off
	v_lshl_add_u64 v[4:5], v[8:9], 0, s[84:85]
	s_mov_b32 m0, s29
	s_add_i32 s30, s24, 0xa000
	global_load_lds_dwordx4 v[4:5], off
	v_lshl_add_u64 v[4:5], v[10:11], 0, s[84:85]
	s_mov_b32 m0, s30
	s_mov_b64 s[12:13], 0
	global_load_lds_dwordx4 v[4:5], off
	s_add_i32 m0, s24, 0x1c000
	v_lshl_add_u64 v[4:5], s[8:9], 0, v[130:131]
	global_load_lds_dwordx4 v[4:5], off
	v_lshl_add_u64 v[4:5], s[8:9], 0, v[132:133]
	s_add_i32 m0, s24, 0x1e000
	s_mov_b64 s[8:9], -1
	global_load_lds_dwordx4 v[4:5], off
	s_waitcnt vmcnt(6)
	s_mov_b64 s[10:11], 0
	v_add_u32_e32 v141, 0, v13
	v_mov_b32_e32 v3, v2
	v_mov_b32_e32 v4, v2
	v_mov_b32_e32 v5, v2
	v_mov_b32_e32 v6, v2
	v_mov_b32_e32 v7, v2
	v_mov_b32_e32 v8, v2
	v_mov_b32_e32 v9, v2
	v_mov_b32_e32 v18, v2
	v_mov_b32_e32 v19, v2
	v_mov_b32_e32 v20, v2
	v_mov_b32_e32 v21, v2
	v_mov_b32_e32 v22, v2
	v_mov_b32_e32 v23, v2
	v_mov_b32_e32 v24, v2
	v_mov_b32_e32 v25, v2
	v_mov_b32_e32 v34, v2
	v_mov_b32_e32 v35, v2
	v_mov_b32_e32 v36, v2
	v_mov_b32_e32 v37, v2
	v_mov_b32_e32 v38, v2
	v_mov_b32_e32 v39, v2
	v_mov_b32_e32 v40, v2
	v_mov_b32_e32 v41, v2
	v_mov_b32_e32 v50, v2
	v_mov_b32_e32 v51, v2
	v_mov_b32_e32 v52, v2
	v_mov_b32_e32 v53, v2
	v_mov_b32_e32 v54, v2
	v_mov_b32_e32 v55, v2
	v_mov_b32_e32 v56, v2
	v_mov_b32_e32 v57, v2
	v_mov_b32_e32 v10, v2
	v_mov_b32_e32 v11, v2
	v_mov_b32_e32 v12, v2
	v_mov_b32_e32 v13, v2
	v_mov_b32_e32 v14, v2
	v_mov_b32_e32 v15, v2
	v_mov_b32_e32 v16, v2
	v_mov_b32_e32 v17, v2
	v_mov_b32_e32 v26, v2
	v_mov_b32_e32 v27, v2
	v_mov_b32_e32 v28, v2
	v_mov_b32_e32 v29, v2
	v_mov_b32_e32 v30, v2
	v_mov_b32_e32 v31, v2
	v_mov_b32_e32 v32, v2
	v_mov_b32_e32 v33, v2
	v_mov_b32_e32 v42, v2
	v_mov_b32_e32 v43, v2
	v_mov_b32_e32 v44, v2
	v_mov_b32_e32 v45, v2
	v_mov_b32_e32 v46, v2
	v_mov_b32_e32 v47, v2
	v_mov_b32_e32 v48, v2
	v_mov_b32_e32 v49, v2
	v_mov_b32_e32 v58, v2
	v_mov_b32_e32 v59, v2
	v_mov_b32_e32 v60, v2
	v_mov_b32_e32 v61, v2
	v_mov_b32_e32 v62, v2
	v_mov_b32_e32 v63, v2
	v_mov_b32_e32 v64, v2
	v_mov_b32_e32 v65, v2
	v_mov_b32_e32 v66, v2
	v_mov_b32_e32 v67, v2
	v_mov_b32_e32 v68, v2
	v_mov_b32_e32 v69, v2
	v_mov_b32_e32 v70, v2
	v_mov_b32_e32 v71, v2
	v_mov_b32_e32 v72, v2
	v_mov_b32_e32 v73, v2
	v_mov_b32_e32 v82, v2
	v_mov_b32_e32 v83, v2
	v_mov_b32_e32 v84, v2
	v_mov_b32_e32 v85, v2
	v_mov_b32_e32 v86, v2
	v_mov_b32_e32 v87, v2
	v_mov_b32_e32 v88, v2
	v_mov_b32_e32 v89, v2
	v_mov_b32_e32 v98, v2
	v_mov_b32_e32 v99, v2
	v_mov_b32_e32 v100, v2
	v_mov_b32_e32 v101, v2
	v_mov_b32_e32 v102, v2
	v_mov_b32_e32 v103, v2
	v_mov_b32_e32 v104, v2
	v_mov_b32_e32 v105, v2
	v_mov_b32_e32 v114, v2
	v_mov_b32_e32 v115, v2
	v_mov_b32_e32 v116, v2
	v_mov_b32_e32 v117, v2
	v_mov_b32_e32 v118, v2
	v_mov_b32_e32 v119, v2
	v_mov_b32_e32 v120, v2
	v_mov_b32_e32 v121, v2
	v_mov_b32_e32 v74, v2
	v_mov_b32_e32 v75, v2
	v_mov_b32_e32 v76, v2
	v_mov_b32_e32 v77, v2
	v_mov_b32_e32 v78, v2
	v_mov_b32_e32 v79, v2
	v_mov_b32_e32 v80, v2
	v_mov_b32_e32 v81, v2
	v_mov_b32_e32 v90, v2
	v_mov_b32_e32 v91, v2
	v_mov_b32_e32 v92, v2
	v_mov_b32_e32 v93, v2
	v_mov_b32_e32 v94, v2
	v_mov_b32_e32 v95, v2
	v_mov_b32_e32 v96, v2
	v_mov_b32_e32 v97, v2
	v_mov_b32_e32 v106, v2
	v_mov_b32_e32 v107, v2
	v_mov_b32_e32 v108, v2
	v_mov_b32_e32 v109, v2
	v_mov_b32_e32 v110, v2
	v_mov_b32_e32 v111, v2
	v_mov_b32_e32 v112, v2
	v_mov_b32_e32 v113, v2
	v_mov_b32_e32 v122, v2
	v_mov_b32_e32 v123, v2
	v_mov_b32_e32 v124, v2
	v_mov_b32_e32 v125, v2
	v_mov_b32_e32 v126, v2
	v_mov_b32_e32 v127, v2
	v_mov_b32_e32 v128, v2
	v_mov_b32_e32 v129, v2
	s_barrier
	.p2align 6

.LBB0_997:
	s_add_u32 s16, s16, 0x40080
	s_addc_u32 s17, s17, 0
	s_add_u32 s11, s18, 0x100
	v_mov_b64_e32 v[8:9], v[4:5]
	v_mov_b64_e32 v[20:21], v[4:5]
	v_mov_b64_e32 v[24:25], v[4:5]
	v_mov_b64_e32 v[36:37], v[4:5]
	v_mov_b64_e32 v[40:41], v[4:5]
	v_mov_b64_e32 v[52:53], v[4:5]
	v_mov_b64_e32 v[56:57], v[4:5]
	v_mov_b64_e32 v[12:13], v[4:5]
	v_mov_b64_e32 v[16:17], v[4:5]
	v_mov_b64_e32 v[28:29], v[4:5]
	v_mov_b64_e32 v[32:33], v[4:5]
	v_mov_b64_e32 v[44:45], v[4:5]
	v_mov_b64_e32 v[48:49], v[4:5]
	v_mov_b64_e32 v[60:61], v[4:5]
	v_mov_b64_e32 v[64:65], v[4:5]
	v_mov_b64_e32 v[84:85], v[4:5]
	v_mov_b64_e32 v[88:89], v[4:5]
	v_mov_b64_e32 v[96:97], v[4:5]
	v_mov_b64_e32 v[100:101], v[4:5]
	v_mov_b64_e32 v[112:113], v[4:5]
	v_mov_b64_e32 v[116:117], v[4:5]
	v_mov_b64_e32 v[128:129], v[4:5]
	v_mov_b64_e32 v[134:135], v[4:5]
	v_mov_b64_e32 v[92:93], v[4:5]
	v_mov_b64_e32 v[104:105], v[4:5]
	v_mov_b64_e32 v[108:109], v[4:5]
	v_mov_b64_e32 v[120:121], v[4:5]
	v_mov_b64_e32 v[124:125], v[4:5]
	v_mov_b64_e32 v[138:139], v[4:5]
	v_mov_b64_e32 v[142:143], v[4:5]
	v_mov_b64_e32 v[146:147], v[4:5]
	s_addc_u32 s36, s19, 0
	s_mov_b32 s37, -2
	v_mov_b64_e32 v[6:7], v[2:3]
	v_mov_b64_e32 v[18:19], v[2:3]
	v_mov_b64_e32 v[22:23], v[2:3]
	v_mov_b64_e32 v[34:35], v[2:3]
	v_mov_b64_e32 v[38:39], v[2:3]
	v_mov_b64_e32 v[50:51], v[2:3]
	v_mov_b64_e32 v[54:55], v[2:3]
	v_mov_b64_e32 v[10:11], v[2:3]
	v_mov_b64_e32 v[14:15], v[2:3]
	v_mov_b64_e32 v[26:27], v[2:3]
	v_mov_b64_e32 v[30:31], v[2:3]
	v_mov_b64_e32 v[42:43], v[2:3]
	v_mov_b64_e32 v[46:47], v[2:3]
	v_mov_b64_e32 v[58:59], v[2:3]
	v_mov_b64_e32 v[62:63], v[2:3]
	v_mov_b64_e32 v[82:83], v[2:3]
	v_mov_b64_e32 v[86:87], v[2:3]
	v_mov_b64_e32 v[94:95], v[2:3]
	v_mov_b64_e32 v[98:99], v[2:3]
	v_mov_b64_e32 v[110:111], v[2:3]
	v_mov_b64_e32 v[114:115], v[2:3]
	v_mov_b64_e32 v[126:127], v[2:3]
	v_mov_b64_e32 v[132:133], v[2:3]
	v_mov_b64_e32 v[90:91], v[2:3]
	v_mov_b64_e32 v[102:103], v[2:3]
	v_mov_b64_e32 v[106:107], v[2:3]
	v_mov_b64_e32 v[118:119], v[2:3]
	v_mov_b64_e32 v[122:123], v[2:3]
	v_mov_b64_e32 v[136:137], v[2:3]
	v_mov_b64_e32 v[140:141], v[2:3]
	v_mov_b64_e32 v[144:145], v[2:3]
	.p2align 6

.LBB0_1009:
	v_lshrrev_b32_e32 v18, 1, v10
	v_and_b32_e32 v143, 24, v18
	s_lshl_b32 s2, s2, 5
	v_mov_b32_e32 v137, v131
	v_and_b32_e32 v142, 15, v10
	v_lshlrev_b32_e32 v18, 1, v143
	v_lshlrev_b32_e32 v10, 2, v10
	s_and_b32 s15, s2, 0x60
	s_add_i32 m0, s10, 0x18000
	v_lshl_add_u64 v[4:5], v[4:5], 0, s[84:85]
	v_lshl_add_u64 v[14:15], s[24:25], 0, v[136:137]
	v_mov_b32_e32 v135, v131
	s_lshl_b32 s14, s3, 6
	v_lshl_or_b32 v18, v142, 6, v18
	s_lshl_b32 s3, s3, 13
	v_and_b32_e32 v10, 32, v10
	s_lshl_b32 s2, s15, 7
	s_waitcnt vmcnt(2)
	s_barrier
	global_load_lds_dwordx4 v[4:5], off
	v_lshl_add_u64 v[4:5], v[6:7], 0, s[84:85]
	s_add_i32 m0, s10, 0x1a000
	s_add_i32 s16, s10, 0x8000
	s_add_i32 s17, s10, 0xa000
	v_lshl_add_u64 v[16:17], s[24:25], 0, v[134:135]
	v_bitop3_b32 v144, v18, s2, v10 bitop3:0xde
	global_load_lds_dwordx4 v[4:5], off
	v_lshl_add_u64 v[4:5], v[14:15], 0, s[84:85]
	s_mov_b32 m0, s16
	s_add_u32 s2, s0, 0x40080
	v_bitop3_b32 v19, v18, s3, v10 bitop3:0xde
	global_load_lds_dwordx4 v[4:5], off
	v_lshl_add_u64 v[4:5], v[16:17], 0, s[84:85]
	s_mov_b32 m0, s17
	s_addc_u32 s3, s1, 0
	global_load_lds_dwordx4 v[4:5], off
	s_add_i32 m0, s10, 0x1c000
	v_lshl_add_u64 v[4:5], s[2:3], 0, v[130:131]
	global_load_lds_dwordx4 v[4:5], off
	v_lshl_add_u64 v[4:5], s[2:3], 0, v[132:133]
	s_add_i32 m0, s10, 0x1e000
	v_readlane_b32 s2, v254, 54
	global_load_lds_dwordx4 v[4:5], off
	v_lshlrev_b32_e32 v4, 14, v12
	v_and_b32_e32 v4, 0xffff8000, v4
	v_lshl_add_u32 v4, v11, 11, v4
	v_and_b32_e32 v5, 1, v12
	v_lshl_or_b32 v4, v5, 6, v4
	v_lshl_add_u32 v4, v13, 1, v4
	v_mov_b32_e32 v5, v131
	v_readlane_b32 s3, v254, 55
	s_waitcnt vmcnt(6)
	s_mov_b32 s20, -2
	v_add_u32_e32 v145, 0, v19
	v_lshl_add_u64 v[138:139], s[2:3], 0, v[4:5]
	v_lshlrev_b32_e32 v4, 14, v3
	v_and_b32_e32 v4, 0xffff8000, v4
	v_lshl_add_u32 v4, v8, 11, v4
	v_and_b32_e32 v3, 1, v3
	v_lshl_or_b32 v3, v3, 6, v4
	v_lshl_add_u32 v4, v9, 1, v3
	v_lshl_add_u64 v[140:141], s[2:3], 0, v[4:5]
	v_readlane_b32 s2, v254, 58
	v_readlane_b32 s3, v255, 36
	s_add_u32 s18, s2, s3
	v_readlane_b32 s2, v254, 59
	s_addc_u32 s19, s2, 0
	s_mov_b64 s[2:3], 0
	v_mov_b32_e32 v3, v2
	v_mov_b32_e32 v4, v2
	v_mov_b32_e32 v5, v2
	v_mov_b32_e32 v6, v2
	v_mov_b32_e32 v7, v2
	v_mov_b32_e32 v8, v2
	v_mov_b32_e32 v9, v2
	v_mov_b32_e32 v10, v2
	v_mov_b32_e32 v11, v2
	v_mov_b32_e32 v12, v2
	v_mov_b32_e32 v13, v2
	v_mov_b32_e32 v18, v2
	v_mov_b32_e32 v19, v2
	v_mov_b32_e32 v20, v2
	v_mov_b32_e32 v21, v2
	v_mov_b32_e32 v26, v2
	v_mov_b32_e32 v27, v2
	v_mov_b32_e32 v28, v2
	v_mov_b32_e32 v29, v2
	v_mov_b32_e32 v34, v2
	v_mov_b32_e32 v35, v2
	v_mov_b32_e32 v36, v2
	v_mov_b32_e32 v37, v2
	v_mov_b32_e32 v42, v2
	v_mov_b32_e32 v43, v2
	v_mov_b32_e32 v44, v2
	v_mov_b32_e32 v45, v2
	v_mov_b32_e32 v50, v2
	v_mov_b32_e32 v51, v2
	v_mov_b32_e32 v52, v2
	v_mov_b32_e32 v53, v2
	v_mov_b32_e32 v14, v2
	v_mov_b32_e32 v15, v2
	v_mov_b32_e32 v16, v2
	v_mov_b32_e32 v17, v2
	v_mov_b32_e32 v22, v2
	v_mov_b32_e32 v23, v2
	v_mov_b32_e32 v24, v2
	v_mov_b32_e32 v25, v2
	v_mov_b32_e32 v30, v2
	v_mov_b32_e32 v31, v2
	v_mov_b32_e32 v32, v2
	v_mov_b32_e32 v33, v2
	v_mov_b32_e32 v38, v2
	v_mov_b32_e32 v39, v2
	v_mov_b32_e32 v40, v2
	v_mov_b32_e32 v41, v2
	v_mov_b32_e32 v46, v2
	v_mov_b32_e32 v47, v2
	v_mov_b32_e32 v48, v2
	v_mov_b32_e32 v49, v2
	v_mov_b32_e32 v54, v2
	v_mov_b32_e32 v55, v2
	v_mov_b32_e32 v56, v2
	v_mov_b32_e32 v57, v2
	v_mov_b32_e32 v58, v2
	v_mov_b32_e32 v59, v2
	v_mov_b32_e32 v60, v2
	v_mov_b32_e32 v61, v2
	v_mov_b32_e32 v62, v2
	v_mov_b32_e32 v63, v2
	v_mov_b32_e32 v64, v2
	v_mov_b32_e32 v65, v2
	v_mov_b32_e32 v66, v2
	v_mov_b32_e32 v67, v2
	v_mov_b32_e32 v68, v2
	v_mov_b32_e32 v69, v2
	v_mov_b32_e32 v70, v2
	v_mov_b32_e32 v71, v2
	v_mov_b32_e32 v72, v2
	v_mov_b32_e32 v73, v2
	v_mov_b32_e32 v74, v2
	v_mov_b32_e32 v75, v2
	v_mov_b32_e32 v76, v2
	v_mov_b32_e32 v77, v2
	v_mov_b32_e32 v82, v2
	v_mov_b32_e32 v83, v2
	v_mov_b32_e32 v84, v2
	v_mov_b32_e32 v85, v2
	v_mov_b32_e32 v90, v2
	v_mov_b32_e32 v91, v2
	v_mov_b32_e32 v92, v2
	v_mov_b32_e32 v93, v2
	v_mov_b32_e32 v98, v2
	v_mov_b32_e32 v99, v2
	v_mov_b32_e32 v100, v2
	v_mov_b32_e32 v101, v2
	v_mov_b32_e32 v106, v2
	v_mov_b32_e32 v107, v2
	v_mov_b32_e32 v108, v2
	v_mov_b32_e32 v109, v2
	v_mov_b32_e32 v114, v2
	v_mov_b32_e32 v115, v2
	v_mov_b32_e32 v116, v2
	v_mov_b32_e32 v117, v2
	v_mov_b32_e32 v78, v2
	v_mov_b32_e32 v79, v2
	v_mov_b32_e32 v80, v2
	v_mov_b32_e32 v81, v2
	v_mov_b32_e32 v86, v2
	v_mov_b32_e32 v87, v2
	v_mov_b32_e32 v88, v2
	v_mov_b32_e32 v89, v2
	v_mov_b32_e32 v94, v2
	v_mov_b32_e32 v95, v2
	v_mov_b32_e32 v96, v2
	v_mov_b32_e32 v97, v2
	v_mov_b32_e32 v102, v2
	v_mov_b32_e32 v103, v2
	v_mov_b32_e32 v104, v2
	v_mov_b32_e32 v105, v2
	v_mov_b32_e32 v110, v2
	v_mov_b32_e32 v111, v2
	v_mov_b32_e32 v112, v2
	v_mov_b32_e32 v113, v2
	v_mov_b32_e32 v118, v2
	v_mov_b32_e32 v119, v2
	v_mov_b32_e32 v120, v2
	v_mov_b32_e32 v121, v2
	v_mov_b32_e32 v122, v2
	v_mov_b32_e32 v123, v2
	v_mov_b32_e32 v124, v2
	v_mov_b32_e32 v125, v2
	v_mov_b32_e32 v126, v2
	v_mov_b32_e32 v127, v2
	v_mov_b32_e32 v128, v2
	v_mov_b32_e32 v129, v2
	v_readlane_b32 s26, v254, 52
	v_readlane_b32 s27, v254, 53
	s_barrier
	.p2align 6

.LBB0_1327:
	v_mov_b32_e32 v139, v131
	v_mov_b32_e32 v137, v131
	s_add_u32 s9, s12, 0x100
	v_mov_b64_e32 v[12:13], v[4:5]
	v_mov_b64_e32 v[20:21], v[4:5]
	v_mov_b64_e32 v[28:29], v[4:5]
	v_mov_b64_e32 v[36:37], v[4:5]
	v_mov_b64_e32 v[44:45], v[4:5]
	v_mov_b64_e32 v[52:53], v[4:5]
	v_mov_b64_e32 v[60:61], v[4:5]
	v_mov_b64_e32 v[8:9], v[4:5]
	v_mov_b64_e32 v[16:17], v[4:5]
	v_mov_b64_e32 v[24:25], v[4:5]
	v_mov_b64_e32 v[32:33], v[4:5]
	v_mov_b64_e32 v[40:41], v[4:5]
	v_mov_b64_e32 v[48:49], v[4:5]
	v_mov_b64_e32 v[56:57], v[4:5]
	v_mov_b64_e32 v[64:65], v[4:5]
	v_mov_b64_e32 v[68:69], v[4:5]
	v_mov_b64_e32 v[76:77], v[4:5]
	v_mov_b64_e32 v[84:85], v[4:5]
	v_mov_b64_e32 v[92:93], v[4:5]
	v_mov_b64_e32 v[100:101], v[4:5]
	v_mov_b64_e32 v[108:109], v[4:5]
	v_mov_b64_e32 v[116:117], v[4:5]
	v_mov_b64_e32 v[124:125], v[4:5]
	v_mov_b64_e32 v[72:73], v[4:5]
	v_mov_b64_e32 v[80:81], v[4:5]
	v_mov_b64_e32 v[88:89], v[4:5]
	v_mov_b64_e32 v[96:97], v[4:5]
	v_mov_b64_e32 v[104:105], v[4:5]
	v_mov_b64_e32 v[112:113], v[4:5]
	v_mov_b64_e32 v[120:121], v[4:5]
	v_mov_b64_e32 v[128:129], v[4:5]
	v_lshl_add_u64 v[144:145], s[40:41], 0, v[136:137]
	v_lshl_add_u64 v[146:147], s[40:41], 0, v[138:139]
	s_addc_u32 s31, s13, 0
	s_mov_b32 s34, -2
	s_mov_b64 s[0:1], 0
	v_mov_b64_e32 v[10:11], v[2:3]
	v_mov_b64_e32 v[18:19], v[2:3]
	v_mov_b64_e32 v[26:27], v[2:3]
	v_mov_b64_e32 v[34:35], v[2:3]
	v_mov_b64_e32 v[42:43], v[2:3]
	v_mov_b64_e32 v[50:51], v[2:3]
	v_mov_b64_e32 v[58:59], v[2:3]
	v_mov_b64_e32 v[6:7], v[2:3]
	v_mov_b64_e32 v[14:15], v[2:3]
	v_mov_b64_e32 v[22:23], v[2:3]
	v_mov_b64_e32 v[30:31], v[2:3]
	v_mov_b64_e32 v[38:39], v[2:3]
	v_mov_b64_e32 v[46:47], v[2:3]
	v_mov_b64_e32 v[54:55], v[2:3]
	v_mov_b64_e32 v[62:63], v[2:3]
	v_mov_b64_e32 v[66:67], v[2:3]
	v_mov_b64_e32 v[74:75], v[2:3]
	v_mov_b64_e32 v[82:83], v[2:3]
	v_mov_b64_e32 v[90:91], v[2:3]
	v_mov_b64_e32 v[98:99], v[2:3]
	v_mov_b64_e32 v[106:107], v[2:3]
	v_mov_b64_e32 v[114:115], v[2:3]
	v_mov_b64_e32 v[122:123], v[2:3]
	v_mov_b64_e32 v[70:71], v[2:3]
	v_mov_b64_e32 v[78:79], v[2:3]
	v_mov_b64_e32 v[86:87], v[2:3]
	v_mov_b64_e32 v[94:95], v[2:3]
	v_mov_b64_e32 v[102:103], v[2:3]
	v_mov_b64_e32 v[110:111], v[2:3]
	v_mov_b64_e32 v[118:119], v[2:3]
	v_mov_b64_e32 v[126:127], v[2:3]
	.p2align 6

.LBB0_1396:
	s_add_u32 s18, s18, 0x80080
	s_addc_u32 s19, s19, 0
	s_add_u32 s9, s20, 0x100
	v_mov_b64_e32 v[8:9], v[4:5]
	v_mov_b64_e32 v[20:21], v[4:5]
	v_mov_b64_e32 v[24:25], v[4:5]
	v_mov_b64_e32 v[36:37], v[4:5]
	v_mov_b64_e32 v[40:41], v[4:5]
	v_mov_b64_e32 v[52:53], v[4:5]
	v_mov_b64_e32 v[56:57], v[4:5]
	v_mov_b64_e32 v[12:13], v[4:5]
	v_mov_b64_e32 v[16:17], v[4:5]
	v_mov_b64_e32 v[28:29], v[4:5]
	v_mov_b64_e32 v[32:33], v[4:5]
	v_mov_b64_e32 v[44:45], v[4:5]
	v_mov_b64_e32 v[48:49], v[4:5]
	v_mov_b64_e32 v[60:61], v[4:5]
	v_mov_b64_e32 v[64:65], v[4:5]
	v_mov_b64_e32 v[68:69], v[4:5]
	v_mov_b64_e32 v[72:73], v[4:5]
	v_mov_b64_e32 v[84:85], v[4:5]
	v_mov_b64_e32 v[88:89], v[4:5]
	v_mov_b64_e32 v[100:101], v[4:5]
	v_mov_b64_e32 v[104:105], v[4:5]
	v_mov_b64_e32 v[116:117], v[4:5]
	v_mov_b64_e32 v[120:121], v[4:5]
	v_mov_b64_e32 v[76:77], v[4:5]
	v_mov_b64_e32 v[80:81], v[4:5]
	v_mov_b64_e32 v[92:93], v[4:5]
	v_mov_b64_e32 v[96:97], v[4:5]
	v_mov_b64_e32 v[108:109], v[4:5]
	v_mov_b64_e32 v[112:113], v[4:5]
	v_mov_b64_e32 v[124:125], v[4:5]
	v_mov_b64_e32 v[128:129], v[4:5]
	s_addc_u32 s11, s21, 0
	s_mov_b32 s38, -2
	v_mov_b64_e32 v[6:7], v[2:3]
	v_mov_b64_e32 v[18:19], v[2:3]
	v_mov_b64_e32 v[22:23], v[2:3]
	v_mov_b64_e32 v[34:35], v[2:3]
	v_mov_b64_e32 v[38:39], v[2:3]
	v_mov_b64_e32 v[50:51], v[2:3]
	v_mov_b64_e32 v[54:55], v[2:3]
	v_mov_b64_e32 v[10:11], v[2:3]
	v_mov_b64_e32 v[14:15], v[2:3]
	v_mov_b64_e32 v[26:27], v[2:3]
	v_mov_b64_e32 v[30:31], v[2:3]
	v_mov_b64_e32 v[42:43], v[2:3]
	v_mov_b64_e32 v[46:47], v[2:3]
	v_mov_b64_e32 v[58:59], v[2:3]
	v_mov_b64_e32 v[62:63], v[2:3]
	v_mov_b64_e32 v[66:67], v[2:3]
	v_mov_b64_e32 v[70:71], v[2:3]
	v_mov_b64_e32 v[82:83], v[2:3]
	v_mov_b64_e32 v[86:87], v[2:3]
	v_mov_b64_e32 v[98:99], v[2:3]
	v_mov_b64_e32 v[102:103], v[2:3]
	v_mov_b64_e32 v[114:115], v[2:3]
	v_mov_b64_e32 v[118:119], v[2:3]
	v_mov_b64_e32 v[74:75], v[2:3]
	v_mov_b64_e32 v[78:79], v[2:3]
	v_mov_b64_e32 v[90:91], v[2:3]
	v_mov_b64_e32 v[94:95], v[2:3]
	v_mov_b64_e32 v[106:107], v[2:3]
	v_mov_b64_e32 v[110:111], v[2:3]
	v_mov_b64_e32 v[122:123], v[2:3]
	v_mov_b64_e32 v[126:127], v[2:3]
	.p2align 6
